# attention: DMA issue at step end plus next-tile row-max tree under the P.V MFMAs (on v11)
# speedup vs baseline: 1.0118x; 1.0047x over previous
; #define ATT_DMAK(tile, slot) do { _Pragma("unroll") for (int i = 0; i < 4; ++i) { const int pc = (wv + 8 * i) < 25 ? (wv + 8 * i) : 24; \
;         __builtin_amdgcn_global_load_lds((const unsigned*)((const char*)Kbh + (size_t)(tile) * (64 * 384) + doffK[i]), (LAS unsigned*)(lds + (slot) * KT_BYTES + pc * 1024), 16, 0, 0); } } while (0)
; #define ATT_DMAV(tile, slot) do { _Pragma("unroll") for (int i = 0; i < 3; ++i) { const int pc = (wv + 8 * i) < 18 ? (wv + 8 * i) : 17; \
;         __builtin_amdgcn_global_load_lds((const unsigned*)((const char*)Vbh + (size_t)(tile) * 128 + doffV[i]), (LAS unsigned*)(lds + VRING + (slot) * VT_BYTES + pc * 1024), 16, 0, 0); } } while (0)
; __device__ __forceinline__ void attn_unit(const bf16_t* Qrows  , const bf16_t* Kbh, const bf16_t* Vbh, int nkeys, bf16_t* Orows, LAS unsigned char* lds) {
;     ...
;         if (j + 4 < nt) ATT_DMAK(j + 4, v0);
;         if (j + 3 < nt) ATT_DMAV(j + 3, v0 == 0 ? 2 : v0 - 1);
.LBB0_1235:
	s_add_i32 s15, s14, 1
	s_cmp_lg_u32 s14, 2
	s_cselect_b32 s14, s15, 0
	s_mul_i32 s15, s14, 0x6400
	v_add_u32_e32 v70, s15, v185
	ds_read_b128 v[66:69], v70
	ds_read_b128 v[166:169], v70 offset:32
	ds_read_b128 v[170:173], v70 offset:64
	ds_read_b128 v[188:191], v70 offset:96
	ds_read_b128 v[192:195], v70 offset:128
	ds_read_b128 v[196:199], v70 offset:160
	ds_read_b128 v[200:203], v70 offset:192
	ds_read_b128 v[216:219], v70 offset:224
	ds_read_b128 v[220:223], v70 offset:256
	ds_read_b128 v[224:227], v70 offset:288
	ds_read_b128 v[228:231], v70 offset:320
	ds_read_b128 v[146:149], v70 offset:352
	s_waitcnt lgkmcnt(11)
	v_mfma_f32_32x32x16_bf16 v[66:81], v[66:69], v[142:145], 0
	v_sub_f32_e32 v82, v82, v183
	v_exp_f32_e32 v82, v82
	v_sub_f32_e32 v94, v94, v183
	v_exp_f32_e32 v94, v94
	v_add_f32_e32 v165, 0, v82
	v_add_f32_e32 v165, v94, v165
	s_waitcnt lgkmcnt(10)
	v_mfma_f32_32x32x16_bf16 v[66:81], v[166:169], v[138:141], v[66:81]
	v_sub_f32_e32 v83, v83, v183
	v_exp_f32_e32 v83, v83
	v_sub_f32_e32 v95, v95, v183
	v_exp_f32_e32 v95, v95
	v_add_f32_e32 v165, v83, v165
	v_cvt_pk_bf16_f32 v82, v82, v83
	v_add_f32_e32 v165, v95, v165
	v_sub_f32_e32 v83, v84, v183
	s_waitcnt lgkmcnt(9)
	v_mfma_f32_32x32x16_bf16 v[66:81], v[170:173], v[134:137], v[66:81]
	v_exp_f32_e32 v83, v83
	v_sub_f32_e32 v96, v96, v183
	v_add_f32_e32 v84, v83, v165
	v_exp_f32_e32 v165, v96
	s_nop 0
	v_add_f32_e32 v84, v165, v84
	s_waitcnt lgkmcnt(8)
	v_mfma_f32_32x32x16_bf16 v[66:81], v[188:191], v[130:133], v[66:81]
	v_sub_f32_e32 v85, v85, v183
	v_exp_f32_e32 v85, v85
	v_sub_f32_e32 v96, v97, v183
	v_exp_f32_e32 v97, v96
	v_cvt_pk_bf16_f32 v96, v94, v95
	v_add_f32_e32 v84, v85, v84
	v_cvt_pk_bf16_f32 v83, v83, v85
	v_add_f32_e32 v84, v97, v84
	v_cvt_pk_bf16_f32 v97, v165, v97
	s_waitcnt lgkmcnt(7)
	v_mfma_f32_32x32x16_bf16 v[66:81], v[192:195], v[126:129], v[66:81]
	v_sub_f32_e32 v85, v86, v183
	v_exp_f32_e32 v85, v85
	s_nop 0
	v_add_f32_e32 v84, v85, v84
	s_waitcnt lgkmcnt(6)
	v_mfma_f32_32x32x16_bf16 v[66:81], v[196:199], v[122:125], v[66:81]
	v_sub_f32_e32 v86, v87, v183
	v_exp_f32_e32 v86, v86
	s_nop 0
	v_add_f32_e32 v87, v86, v84
	v_cvt_pk_bf16_f32 v84, v85, v86
	s_waitcnt lgkmcnt(5)
	v_mfma_f32_32x32x16_bf16 v[66:81], v[200:203], v[118:121], v[66:81]
	v_sub_f32_e32 v85, v88, v183
	v_exp_f32_e32 v85, v85
	s_nop 0
	v_add_f32_e32 v86, v85, v87
	s_waitcnt lgkmcnt(4)
	v_mfma_f32_32x32x16_bf16 v[66:81], v[216:219], v[114:117], v[66:81]
	v_sub_f32_e32 v87, v89, v183
	v_exp_f32_e32 v87, v87
	s_nop 0
	v_add_f32_e32 v86, v87, v86
	v_cvt_pk_bf16_f32 v85, v85, v87
	v_sub_f32_e32 v87, v90, v183
	v_exp_f32_e32 v90, v87
	s_waitcnt lgkmcnt(3)
	v_mfma_f32_32x32x16_bf16 v[66:81], v[220:223], v[110:113], v[66:81]
	v_add_u32_e32 v165, s13, v187
	v_add_f32_e32 v94, v90, v86
	ds_read_b128 v[86:89], v165
	ds_read_b128 v[166:169], v165 offset:32
	s_waitcnt lgkmcnt(4)
	v_mfma_f32_32x32x16_bf16 v[66:81], v[224:227], v[106:109], v[66:81]
	v_sub_f32_e32 v91, v91, v183
	ds_read_b128 v[170:173], v165 offset:4608
	ds_read_b128 v[188:191], v165 offset:4640
	v_exp_f32_e32 v91, v91
	s_nop 0
	v_add_f32_e32 v95, v91, v94
	v_cvt_pk_bf16_f32 v94, v90, v91
	s_waitcnt lgkmcnt(5)
	v_mfma_f32_32x32x16_bf16 v[66:81], v[228:231], v[102:105], v[66:81]
	v_sub_f32_e32 v90, v92, v183
	ds_read_b128 v[192:195], v165 offset:9216
	ds_read_b128 v[196:199], v165 offset:9248
	v_exp_f32_e32 v90, v90
	s_nop 0
	v_add_f32_e32 v91, v90, v95
	v_sub_f32_e32 v92, v93, v183
	v_exp_f32_e32 v92, v92
	s_waitcnt lgkmcnt(6)
	v_mfma_f32_32x32x16_bf16 v[66:81], v[146:149], v[98:101], v[66:81]
	v_add_f32_e32 v186, v92, v91
	v_cvt_pk_bf16_f32 v95, v90, v92
	ds_read_b128 v[90:93], v165 offset:13824
	ds_read_b128 v[146:149], v165 offset:13856
	s_waitcnt lgkmcnt(0)
	v_mfma_f32_32x32x16_bf16 v[50:65], v[86:89], v[82:85], v[50:65]
	v_add_f32_e32 v186, v164, v186
	v_mfma_f32_32x32x16_bf16 v[34:49], v[170:173], v[82:85], v[34:49]
	v_mfma_f32_32x32x16_bf16 v[18:33], v[192:195], v[82:85], v[18:33]
	v_max_f32_e32 v150, v66, v67
	v_max3_f32 v150, v150, v68, v69
	v_mfma_f32_32x32x16_bf16 v[2:17], v[90:93], v[82:85], v[2:17]
	v_max3_f32 v150, v150, v70, v71
	v_max3_f32 v150, v150, v72, v73
	v_mfma_f32_32x32x16_bf16 v[50:65], v[166:169], v[94:97], v[50:65]
	v_max3_f32 v150, v150, v74, v75
	v_max3_f32 v150, v150, v76, v77
	v_mfma_f32_32x32x16_bf16 v[34:49], v[188:191], v[94:97], v[34:49]
	v_max3_f32 v150, v150, v78, v79
	v_max3_f32 v150, v150, v80, v81
	v_mfma_f32_32x32x16_bf16 v[18:33], v[196:199], v[94:97], v[18:33]
	v_mfma_f32_32x32x16_bf16 v[2:17], v[146:149], v[94:97], v[2:17]
	v_mov_b32_e32 v151, v150
	s_nop 1
	v_permlane32_swap_b32_e32 v151, v150
	v_max_f32_e32 v150, v150, v151
	s_and_b64 vcc, exec, s[0:1]
	s_cbranch_vccnz .LattB_v
	s_mul_i32 s13, s12, 0x6400
	s_add_i32 s13, s13, 0
	s_add_u32 s16, s80, s2
	s_addc_u32 s17, s81, s3
	s_add_u32 s16, s16, 0x30e90000
	s_addc_u32 s17, s17, 0
	s_add_i32 m0, s13, s65
	s_nop 0
	global_load_lds_dwordx4 v208, s[16:17]
	s_add_i32 m0, s13, s66
	s_nop 0
	global_load_lds_dwordx4 v209, s[16:17]
	s_add_i32 m0, s13, s67
	s_add_i32 s13, s13, s68
	global_load_lds_dwordx4 v210, s[16:17]
	s_add_i32 m0, s13, 0x6000
	s_nop 0
	global_load_lds_dwordx4 v211, s[16:17]

; #define ATT_DMAK(tile, slot) do { _Pragma("unroll") for (int i = 0; i < 4; ++i) { const int pc = (wv + 8 * i) < 25 ? (wv + 8 * i) : 24; \
;         __builtin_amdgcn_global_load_lds((const unsigned*)((const char*)Kbh + (size_t)(tile) * (64 * 384) + doffK[i]), (LAS unsigned*)(lds + (slot) * KT_BYTES + pc * 1024), 16, 0, 0); } } while (0)
; #define ATT_DMAV(tile, slot) do { _Pragma("unroll") for (int i = 0; i < 3; ++i) { const int pc = (wv + 8 * i) < 18 ? (wv + 8 * i) : 17; \
;         __builtin_amdgcn_global_load_lds((const unsigned*)((const char*)Vbh + (size_t)(tile) * 128 + doffV[i]), (LAS unsigned*)(lds + VRING + (slot) * VT_BYTES + pc * 1024), 16, 0, 0); } } while (0)
; #define ATT_SYNC(full) do { if (full) asm volatile("s_waitcnt vmcnt(7)" ::: "memory"); else asm volatile("s_waitcnt vmcnt(0)" ::: "memory"); \
;         __builtin_amdgcn_s_barrier(); asm volatile("" ::: "memory"); } while (0)
; __device__ __forceinline__ void attn_unit(const bf16_t* Qrows  , const bf16_t* Kbh, const bf16_t* Vbh, int nkeys, bf16_t* Orows, LAS unsigned char* lds) {
;     ...
;         ATT_SYNC(true);
;         if (j + 3 < nt) ATT_DMAK(j + 3, v0);
;         ATT_DMAV(j + 2, v0 == 0 ? 2 : v0 - 1);
;         ATT_STEP(sA, sB, true, k1, v0);
.LBB0_1236:
	s_add_i32 s0, s63, -1
	s_cmp_lt_u32 s0, s64
	s_waitcnt vmcnt(7)
	s_barrier
	s_cselect_b64 s[24:25], -1, 0
	s_cmp_ge_u32 s0, s64
	s_cselect_b64 s[0:1], -1, 0
	s_mul_i32 s12, s36, 0x4800
	v_mov_b32_e32 v82, v150
	v_add_f32_e32 v83, 0x41000000, v183
	v_cmp_gt_f32_e32 vcc, v82, v83
	s_cbranch_vccz .LBB0_1240
	v_max_f32_e32 v82, v82, v82
	v_max_f32_e32 v83, v183, v183
	v_max_f32_e32 v83, v83, v82
	v_sub_f32_e32 v82, v183, v83
	v_exp_f32_e32 v82, v82
	v_mov_b32_e32 v183, v83
	v_pk_mul_f32 v[64:65], v[64:65], v[82:83] op_sel_hi:[1,0]
	v_pk_mul_f32 v[62:63], v[62:63], v[82:83] op_sel_hi:[1,0]
	v_pk_mul_f32 v[60:61], v[60:61], v[82:83] op_sel_hi:[1,0]
	v_pk_mul_f32 v[58:59], v[58:59], v[82:83] op_sel_hi:[1,0]
	v_pk_mul_f32 v[56:57], v[56:57], v[82:83] op_sel_hi:[1,0]
	v_pk_mul_f32 v[54:55], v[54:55], v[82:83] op_sel_hi:[1,0]
	v_pk_mul_f32 v[52:53], v[52:53], v[82:83] op_sel_hi:[1,0]
	v_pk_mul_f32 v[50:51], v[50:51], v[82:83] op_sel_hi:[1,0]
	v_pk_mul_f32 v[48:49], v[48:49], v[82:83] op_sel_hi:[1,0]
	v_pk_mul_f32 v[46:47], v[46:47], v[82:83] op_sel_hi:[1,0]
	v_pk_mul_f32 v[44:45], v[44:45], v[82:83] op_sel_hi:[1,0]
	v_pk_mul_f32 v[42:43], v[42:43], v[82:83] op_sel_hi:[1,0]
	v_pk_mul_f32 v[40:41], v[40:41], v[82:83] op_sel_hi:[1,0]
	v_pk_mul_f32 v[38:39], v[38:39], v[82:83] op_sel_hi:[1,0]
	v_pk_mul_f32 v[36:37], v[36:37], v[82:83] op_sel_hi:[1,0]
	v_pk_mul_f32 v[34:35], v[34:35], v[82:83] op_sel_hi:[1,0]
	v_pk_mul_f32 v[32:33], v[32:33], v[82:83] op_sel_hi:[1,0]
	v_pk_mul_f32 v[30:31], v[30:31], v[82:83] op_sel_hi:[1,0]
	v_pk_mul_f32 v[28:29], v[28:29], v[82:83] op_sel_hi:[1,0]
	v_pk_mul_f32 v[26:27], v[26:27], v[82:83] op_sel_hi:[1,0]
	v_pk_mul_f32 v[24:25], v[24:25], v[82:83] op_sel_hi:[1,0]
	v_pk_mul_f32 v[22:23], v[22:23], v[82:83] op_sel_hi:[1,0]
	v_pk_mul_f32 v[20:21], v[20:21], v[82:83] op_sel_hi:[1,0]
	v_pk_mul_f32 v[18:19], v[18:19], v[82:83] op_sel_hi:[1,0]
	v_pk_mul_f32 v[16:17], v[16:17], v[82:83] op_sel_hi:[1,0]
	v_pk_mul_f32 v[14:15], v[14:15], v[82:83] op_sel_hi:[1,0]
	v_pk_mul_f32 v[12:13], v[12:13], v[82:83] op_sel_hi:[1,0]
	v_pk_mul_f32 v[10:11], v[10:11], v[82:83] op_sel_hi:[1,0]
	v_pk_mul_f32 v[8:9], v[8:9], v[82:83] op_sel_hi:[1,0]
	v_pk_mul_f32 v[6:7], v[6:7], v[82:83] op_sel_hi:[1,0]
	v_pk_mul_f32 v[4:5], v[4:5], v[82:83] op_sel_hi:[1,0]
	v_pk_mul_f32 v[2:3], v[2:3], v[82:83] op_sel_hi:[1,0]
	v_mul_f32_e32 v186, v186, v82
.LBB0_1240:
	s_mul_i32 s13, s14, 0x6400
	v_add_u32_e32 v86, s13, v185
	ds_read_b128 v[82:85], v86
	ds_read_b128 v[188:191], v86 offset:32
	ds_read_b128 v[192:195], v86 offset:64
	ds_read_b128 v[196:199], v86 offset:96
	ds_read_b128 v[200:203], v86 offset:128
	ds_read_b128 v[216:219], v86 offset:160
	ds_read_b128 v[220:223], v86 offset:192
	ds_read_b128 v[224:227], v86 offset:224
	ds_read_b128 v[228:231], v86 offset:256
	ds_read_b128 v[232:235], v86 offset:288
	ds_read_b128 v[236:239], v86 offset:320
	ds_read_b128 v[240:243], v86 offset:352
	s_waitcnt lgkmcnt(11)
	v_mfma_f32_32x32x16_bf16 v[82:97], v[82:85], v[142:145], 0
	v_sub_f32_e32 v66, v66, v183
	v_sub_f32_e32 v78, v78, v183
	v_exp_f32_e32 v66, v66
	v_exp_f32_e32 v78, v78
	s_waitcnt lgkmcnt(10)
	v_mfma_f32_32x32x16_bf16 v[82:97], v[188:191], v[138:141], v[82:97]
	v_sub_f32_e32 v67, v67, v183
	v_sub_f32_e32 v79, v79, v183
	v_exp_f32_e32 v67, v67
	v_exp_f32_e32 v79, v79
	v_cvt_pk_bf16_f32 v188, v66, v67
	s_waitcnt lgkmcnt(9)
	v_mfma_f32_32x32x16_bf16 v[82:97], v[192:195], v[134:137], v[82:97]
	v_sub_f32_e32 v68, v68, v183
	v_sub_f32_e32 v80, v80, v183
	v_exp_f32_e32 v68, v68
	v_exp_f32_e32 v80, v80
	s_waitcnt lgkmcnt(8)
	v_mfma_f32_32x32x16_bf16 v[82:97], v[196:199], v[130:133], v[82:97]
	v_sub_f32_e32 v69, v69, v183
	v_sub_f32_e32 v81, v81, v183
	v_exp_f32_e32 v69, v69
	v_exp_f32_e32 v81, v81
	v_cvt_pk_bf16_f32 v194, v78, v79
	v_cvt_pk_bf16_f32 v189, v68, v69
	v_cvt_pk_bf16_f32 v195, v80, v81
	s_waitcnt lgkmcnt(7)
	v_mfma_f32_32x32x16_bf16 v[82:97], v[200:203], v[126:129], v[82:97]
	v_sub_f32_e32 v70, v70, v183
	v_exp_f32_e32 v70, v70
	s_waitcnt lgkmcnt(6)
	v_mfma_f32_32x32x16_bf16 v[82:97], v[216:219], v[122:125], v[82:97]
	v_sub_f32_e32 v71, v71, v183
	v_exp_f32_e32 v71, v71
	s_nop 0
	v_cvt_pk_bf16_f32 v190, v70, v71
	s_waitcnt lgkmcnt(5)
	v_mfma_f32_32x32x16_bf16 v[82:97], v[220:223], v[118:121], v[82:97]
	v_sub_f32_e32 v72, v72, v183
	v_exp_f32_e32 v72, v72
	s_waitcnt lgkmcnt(4)
	v_mfma_f32_32x32x16_bf16 v[82:97], v[224:227], v[114:117], v[82:97]
	v_sub_f32_e32 v73, v73, v183
	v_exp_f32_e32 v73, v73
	s_nop 0
	v_cvt_pk_bf16_f32 v191, v72, v73
	s_waitcnt lgkmcnt(3)
	v_mfma_f32_32x32x16_bf16 v[82:97], v[228:231], v[110:113], v[82:97]
	v_add_u32_e32 v204, s12, v187
	v_sub_f32_e32 v74, v74, v183
	ds_read_b128 v[196:199], v204
	ds_read_b128 v[200:203], v204 offset:32
	v_exp_f32_e32 v74, v74
	s_waitcnt lgkmcnt(4)
	v_mfma_f32_32x32x16_bf16 v[82:97], v[232:235], v[106:109], v[82:97]
	v_sub_f32_e32 v75, v75, v183
	ds_read_b128 v[216:219], v204 offset:4608
	ds_read_b128 v[220:223], v204 offset:4640
	v_exp_f32_e32 v75, v75
	s_nop 0
	v_cvt_pk_bf16_f32 v192, v74, v75
	s_waitcnt lgkmcnt(5)
	v_mfma_f32_32x32x16_bf16 v[82:97], v[236:239], v[102:105], v[82:97]
	v_sub_f32_e32 v76, v76, v183
	ds_read_b128 v[224:227], v204 offset:9216
	ds_read_b128 v[228:231], v204 offset:9248
	v_exp_f32_e32 v76, v76
	s_waitcnt lgkmcnt(6)
	v_mfma_f32_32x32x16_bf16 v[82:97], v[240:243], v[98:101], v[82:97]
	v_sub_f32_e32 v77, v77, v183
	ds_read_b128 v[232:235], v204 offset:13824
	ds_read_b128 v[236:239], v204 offset:13856
	v_exp_f32_e32 v77, v77
	s_nop 0
	v_cvt_pk_bf16_f32 v193, v76, v77
	s_waitcnt lgkmcnt(0)
	v_mfma_f32_32x32x16_bf16 v[50:65], v[196:199], v[188:191], v[50:65]
	v_mfma_f32_32x32x16_bf16 v[34:49], v[216:219], v[188:191], v[34:49]
	v_mfma_f32_32x32x16_bf16 v[18:33], v[224:227], v[188:191], v[18:33]
	v_max_f32_e32 v152, v82, v83
	v_max3_f32 v152, v152, v84, v85
	v_mfma_f32_32x32x16_bf16 v[2:17], v[232:235], v[188:191], v[2:17]
	v_max3_f32 v152, v152, v86, v87
	v_max3_f32 v152, v152, v88, v89
	v_mfma_f32_32x32x16_bf16 v[50:65], v[200:203], v[192:195], v[50:65]
	v_max3_f32 v152, v152, v90, v91
	v_max3_f32 v152, v152, v92, v93
	v_mfma_f32_32x32x16_bf16 v[34:49], v[220:223], v[192:195], v[34:49]
	v_max3_f32 v152, v152, v94, v95
	v_max3_f32 v152, v152, v96, v97
	v_mfma_f32_32x32x16_bf16 v[18:33], v[228:231], v[192:195], v[18:33]
	v_mfma_f32_32x32x16_bf16 v[2:17], v[236:239], v[192:195], v[2:17]
	v_mov_b32_e32 v153, v152
	s_nop 1
	v_permlane32_swap_b32_e32 v153, v152
	v_max_f32_e32 v152, v152, v153
	s_and_b64 vcc, exec, s[0:1]
	s_cbranch_vccnz .LattA_v
	s_mul_i32 s12, s36, 0x6400
	s_add_i32 s12, s12, 0
	s_add_u32 s16, s80, s2
	s_addc_u32 s17, s81, s3
	s_add_u32 s16, s16, 0x30e8a000
	s_addc_u32 s17, s17, 0
	s_add_i32 m0, s12, s65
	s_nop 0
	global_load_lds_dwordx4 v208, s[16:17]
	s_add_i32 m0, s12, s66
	s_nop 0
	global_load_lds_dwordx4 v209, s[16:17]
	s_add_i32 m0, s12, s67
	s_add_i32 s12, s12, s68
	global_load_lds_dwordx4 v210, s[16:17]
	s_add_i32 m0, s12, 0x6000
	s_nop 0
	global_load_lds_dwordx4 v211, s[16:17]
